# speedup vs baseline: 1.0386x; 1.0386x over previous
.LBB3_2:
	s_or_b64 exec, exec, s[4:5]
	s_load_dwordx2 s[18:19], s[0:1], 0x8
	s_load_dwordx4 s[4:7], s[0:1], 0x18
	s_movk_i32 s8, 0x100
	v_cmp_gt_u32_e64 s[50:51], s8, v0
	s_and_saveexec_b64 s[8:9], s[50:51]
	v_mov_b32_e32 v1, 0x21e00
	v_lshl_add_u32 v1, v0, 2, v1
	v_mov_b32_e32 v2, 0
	ds_write_b32 v1, v2
	s_or_b64 exec, exec, s[8:9]
	v_cmp_eq_u32_e32 vcc, 0, v0
	s_and_saveexec_b64 s[8:9], vcc
	v_mov_b32_e32 v1, 0
	v_mov_b32_e32 v2, 0x22c50
	ds_write_b32 v2, v1
	s_or_b64 exec, exec, s[8:9]
	v_and_b32_e32 v18, 63, v0
	v_lshlrev_b32_e32 v1, 3, v18
	s_lshl_b32 s30, s3, 2
	s_waitcnt lgkmcnt(0)
	global_load_dwordx2 v[12:13], v1, s[4:5] offset:1024
	global_load_dwordx2 v[6:7], v1, s[4:5] offset:1536
	global_load_dwordx2 v[14:15], v1, s[4:5]
	global_load_dwordx2 v[16:17], v1, s[6:7]
	global_load_dwordx2 v[8:9], v1, s[4:5] offset:512
	global_load_dwordx2 v[10:11], v1, s[6:7] offset:512
	s_movk_i32 s34, 0x100
	v_cmp_gt_u32_e32 vcc, s34, v0
	s_and_saveexec_b64 s[34:35], vcc
	s_cbranch_execz .Lskip_wld
	v_lshlrev_b32_e32 v61, 2, v0
	global_load_dword v64, v61, s[4:5]
	global_load_dword v65, v61, s[4:5] offset:1024
	global_load_dword v66, v61, s[6:7]
.Lskip_wld:
	s_or_b64 exec, exec, s[34:35]
	s_movk_i32 s34, 0x1c0
	v_cmp_gt_u32_e32 vcc, s34, v0
	v_mov_b32_e32 v62, 223
	v_mov_b32_e32 v63, 0x24160
	v_cndmask_b32_e32 v62, 0, v62, vcc
	v_lshl_add_u32 v63, v0, 2, v63
	s_movk_i32 s34, 0x1c2
	v_cmp_gt_u32_e32 vcc, s34, v0
	s_and_saveexec_b64 s[34:35], vcc
	ds_write_b32 v63, v62
	s_or_b64 exec, exec, s[34:35]
	s_add_i32 s4, s30, 0x228a0
	v_mov_b32_e32 v2, s4
	s_barrier
	v_mov_b32_e32 v1, 0x228a0
	ds_read_b32 v2, v2
	ds_read_b32 v20, v1
	v_or_b32_e32 v23, 0x400, v0
	v_or_b32_e32 v22, 0x800, v0
	v_or_b32_e32 v21, 0xc00, v0
	s_waitcnt lgkmcnt(1)
	v_readfirstlane_b32 s4, v2
	s_waitcnt lgkmcnt(0)
	v_readfirstlane_b32 s5, v20
	s_sub_i32 s25, s4, s5
	v_cmp_gt_i32_e32 vcc, s25, v0
	v_cmp_gt_i32_e64 s[6:7], s25, v23
	v_cmp_gt_i32_e64 s[8:9], s25, v22
	v_cndmask_b32_e32 v1, 0, v0, vcc
	v_add_u32_e32 v2, v1, v20
	v_cndmask_b32_e64 v1, 0, v23, s[6:7]
	v_add_u32_e32 v4, v1, v20
	v_cndmask_b32_e64 v1, 0, v22, s[8:9]
	v_add_u32_e32 v24, v1, v20
	v_cmp_gt_i32_e64 s[10:11], s25, v21
	v_ashrrev_i32_e32 v25, 31, v24
	v_ashrrev_i32_e32 v3, 31, v2
	v_cndmask_b32_e64 v1, 0, v21, s[10:11]
	v_lshl_add_u64 v[30:31], v[24:25], 2, s[18:19]
	v_add_u32_e32 v24, v1, v20
	v_lshl_add_u64 v[2:3], v[2:3], 2, s[18:19]
	v_ashrrev_i32_e32 v5, 31, v4
	v_ashrrev_i32_e32 v25, 31, v24
	v_lshl_add_u64 v[4:5], v[4:5], 2, s[18:19]
	v_lshl_add_u64 v[32:33], v[24:25], 2, s[18:19]
	global_load_dword v25, v[2:3], off
	global_load_dword v26, v[4:5], off
	global_load_dword v28, v[30:31], off
	global_load_dword v29, v[32:33], off
	v_cmp_gt_i32_e64 s[4:5], s3, v0
	s_and_saveexec_b64 s[12:13], s[4:5]
	s_cbranch_execz .LBB3_8
	v_lshlrev_b32_e32 v1, 2, v0
	v_add_u32_e32 v2, 0x228a0, v1
	ds_read2_b32 v[2:3], v2 offset1:1
	v_add_u32_e32 v1, 0x22580, v1
	s_waitcnt lgkmcnt(0)
	v_sub_u32_e32 v2, v3, v2
	v_add_u32_e32 v2, 3, v2
	v_ashrrev_i32_e32 v2, 2, v2
	ds_write_b32 v1, v2

.LBB3_39:
	v_cvt_f16_f32_e32 v3, v14
	v_cvt_f16_f32_e32 v4, v12
	v_mul_f32_e32 v21, v16, v2
	v_fma_mixlo_f16 v5, v16, v2, 0
	v_mul_u32_u24_e32 v16, 0x10001, v3
	v_mul_u32_u24_e32 v22, 0x10001, v4
	v_cvt_f16_f32_e32 v3, v15
	v_cvt_f16_f32_e32 v4, v13
	s_mov_b32 s0, 0x10001
	v_mul_u32_u24_sdwa v23, v5, s0 dst_sel:DWORD dst_unused:UNUSED_PAD src0_sel:WORD_0 src1_sel:DWORD
	v_mul_f32_e32 v24, v17, v2
	v_fma_mixlo_f16 v5, v17, v2, 0
	v_mul_u32_u24_e32 v17, 0x10001, v3
	v_mul_u32_u24_e32 v25, 0x10001, v4
	v_cvt_f16_f32_e32 v3, v8
	v_cvt_f16_f32_e32 v4, v6
	v_mul_u32_u24_sdwa v26, v5, s0 dst_sel:DWORD dst_unused:UNUSED_PAD src0_sel:WORD_0 src1_sel:DWORD
	v_mul_f32_e32 v27, v10, v2
	v_fma_mixlo_f16 v5, v10, v2, 0
	v_mul_u32_u24_e32 v10, 0x10001, v3
	v_mul_u32_u24_e32 v28, 0x10001, v4
	v_cvt_f16_f32_e32 v3, v9
	v_cvt_f16_f32_e32 v4, v7
	v_sub_u32_e32 v20, 0x7f000000, v2
	v_mul_f32_e32 v14, v14, v2
	v_mul_f32_e32 v12, v12, v2
	v_mul_f32_e32 v15, v15, v2
	v_mul_f32_e32 v13, v13, v2
	v_mul_u32_u24_sdwa v29, v5, s0 dst_sel:DWORD dst_unused:UNUSED_PAD src0_sel:WORD_0 src1_sel:DWORD
	v_mul_f32_e32 v8, v8, v2
	v_mul_f32_e32 v6, v6, v2
	v_mul_f32_e32 v30, v11, v2
	v_fma_mixlo_f16 v5, v11, v2, 0
	v_mul_f32_e32 v9, v9, v2
	v_mul_f32_e32 v7, v7, v2
	v_cndmask_b32_e64 v2, 0, 1, s[26:27]
	v_mul_u32_u24_e32 v11, 0x10001, v3
	v_mul_u32_u24_e32 v31, 0x10001, v4
	v_mul_u32_u24_sdwa v32, v5, s0 dst_sel:DWORD dst_unused:UNUSED_PAD src0_sel:WORD_0 src1_sel:DWORD
	v_lshlrev_b32_e32 v33, 1, v33
	v_mov_b32_e32 v34, 0x22c50
	v_cmp_ne_u32_e64 s[6:7], 1, v2
	s_movk_i32 s12, 0x3c00
	v_mov_b32_e32 v35, 0x3c00
	s_movk_i32 s34, 0x100
	v_cmp_gt_u32_e32 vcc, s34, v0
	s_and_saveexec_b64 s[34:35], vcc
	s_cbranch_execz .Lskip_stage
	s_waitcnt vmcnt(0)
	v_cvt_pk_f16_f32 v64, v64, v65
	v_lshlrev_b32_e32 v63, 2, v0
	v_add_u32_e32 v63, 0x24870, v63
	ds_write_b32 v63, v64
	ds_write_b32 v63, v66 offset:1024
.Lskip_stage:
	s_or_b64 exec, exec, s[34:35]
	s_waitcnt lgkmcnt(0)
	s_barrier
	s_and_b64 vcc, exec, s[6:7]
	s_cbranch_vccz .LBB3_43
	v_sub_u32_e32 v61, 0x7f000000, v20
	v_and_b32_e32 v63, 31, v18
	v_lshlrev_b32_e32 v10, 2, v63
	v_add_u32_e32 v10, 0x24870, v10
	ds_read_b32 v64, v10 offset:0
	ds_read_b32 v66, v10 offset:1024
	ds_read_b32 v68, v10 offset:128
	ds_read_b32 v70, v10 offset:1152
	ds_read_b32 v72, v10 offset:256
	ds_read_b32 v74, v10 offset:1280
	ds_read_b32 v76, v10 offset:384
	ds_read_b32 v78, v10 offset:1408
	ds_read_b32 v80, v10 offset:512
	ds_read_b32 v82, v10 offset:1536
	ds_read_b32 v84, v10 offset:640
	ds_read_b32 v86, v10 offset:1664
	ds_read_b32 v88, v10 offset:768
	ds_read_b32 v90, v10 offset:1792
	ds_read_b32 v92, v10 offset:896
	ds_read_b32 v94, v10 offset:1920
	s_waitcnt lgkmcnt(0)
	v_mul_f32_e32 v66, v61, v66
	v_cvt_pk_f16_f32 v65, v66, 0
	v_mov_b32_e32 v66, 0
	v_mov_b32_e32 v67, 0
	v_mul_f32_e32 v70, v61, v70
	v_cvt_pk_f16_f32 v69, v70, 0
	v_mov_b32_e32 v70, 0
	v_mov_b32_e32 v71, 0
	v_mul_f32_e32 v74, v61, v74
	v_cvt_pk_f16_f32 v73, v74, 0
	v_mov_b32_e32 v74, 0
	v_mov_b32_e32 v75, 0
	v_mul_f32_e32 v78, v61, v78
	v_cvt_pk_f16_f32 v77, v78, 0
	v_mov_b32_e32 v78, 0
	v_mov_b32_e32 v79, 0
	v_mul_f32_e32 v82, v61, v82
	v_cvt_pk_f16_f32 v81, v82, 0
	v_mov_b32_e32 v82, 0
	v_mov_b32_e32 v83, 0
	v_mul_f32_e32 v86, v61, v86
	v_cvt_pk_f16_f32 v85, v86, 0
	v_mov_b32_e32 v86, 0
	v_mov_b32_e32 v87, 0
	v_mul_f32_e32 v90, v61, v90
	v_cvt_pk_f16_f32 v89, v90, 0
	v_mov_b32_e32 v90, 0
	v_mov_b32_e32 v91, 0
	v_mul_f32_e32 v94, v61, v94
	v_cvt_pk_f16_f32 v93, v94, 0
	v_mov_b32_e32 v94, 0
	v_mov_b32_e32 v95, 0
	v_and_b32_e32 v63, 31, v18
	v_lshrrev_b32_e32 v55, 3, v63
	v_lshlrev_b32_e32 v56, 2, v55
	v_and_b32_e32 v57, 3, v63
	v_add_u32_e32 v56, v56, v57
	v_lshlrev_b32_e32 v55, 4, v55
	v_bfe_u32 v57, v63, 1, 1
	v_lshl_add_u32 v55, v57, 3, v55
	v_and_b32_e32 v57, 1, v63
	v_cmp_eq_u32_e32 vcc, 1, v57
	v_mov_b32_e32 v57, 0x5040100
	v_mov_b32_e32 v10, 0x7060302
	v_lshlrev_b32_e32 v58, 1, v63
	v_cndmask_b32_e32 v57, v57, v10, vcc
	v_mov_b32_e32 v59, 0x22c50
	v_mov_b32_e32 v60, 1
	v_mov_b32_e32 v62, 0x3c003c00
	v_mov_b32_e32 v34, 0
	v_mov_b32_e32 v35, 0
	s_mov_b32 s54, 0xf0f0f0f0
	s_mov_b32 s55, 0
	s_mov_b32 s56, 0
	s_mov_b32 s57, -1
	s_mov_b32 s64, 0x24160
	s_mov_b32 s65, 0x244e0
	s_movk_i32 s49, 0x210
	v_lshrrev_b32_e32 v10, 2, v0
	v_and_b32_e32 v17, 3, v0
	v_mov_b32_e32 v40, 0
	v_mov_b32_e32 v41, 0
	v_mov_b32_e32 v42, 0
	v_mov_b32_e32 v43, 0
	v_cmp_gt_u32_e32 vcc, s3, v10
	s_and_saveexec_b64 s[58:59], vcc
	s_cbranch_execz .Llin_skip
	v_lshlrev_b32_e32 v11, 2, v10
	v_add_u32_e32 v12, 0x228a0, v11
	v_add_u32_e32 v13, 0x22580, v11
	ds_read2_b32 v[14:15], v12 offset1:1
	ds_read_b32 v43, v13
	s_waitcnt lgkmcnt(0)
	v_sub_u32_e32 v42, v15, v14
	v_add_u32_e32 v14, 3, v42
	v_lshrrev_b32_e32 v14, 2, v14
	v_add_u32_e32 v15, v43, v14
	v_add_u32_e32 v16, v43, v17
	v_mov_b32_e32 v13, 0x1ce00
.Llin_loop:
	v_cmp_lt_u32_e32 vcc, v16, v15
	s_and_b64 exec, exec, vcc
	s_cbranch_execz .Llin_skip
	v_lshl_add_u32 v12, v16, 4, v13
	ds_read_b128 v[36:39], v12
	v_add_u32_e32 v16, 4, v16
	s_waitcnt lgkmcnt(0)
	v_dot2_f32_f16 v40, v36, v62, v40
	v_dot2_f32_f16 v41, v37, v62, v41
	v_dot2_f32_f16 v40, v38, v62, v40
	v_dot2_f32_f16 v41, v39, v62, v41
	s_branch .Llin_loop
.Llin_skip:
	s_mov_b64 exec, s[58:59]
	s_nop 4
	v_add_f32_dpp v40, v40, v40 quad_perm:[1,0,3,2] row_mask:0xf bank_mask:0xf
	v_add_f32_dpp v41, v41, v41 quad_perm:[1,0,3,2] row_mask:0xf bank_mask:0xf
	s_nop 1
	v_add_f32_dpp v40, v40, v40 quad_perm:[2,3,0,1] row_mask:0xf bank_mask:0xf
	v_add_f32_dpp v41, v41, v41 quad_perm:[2,3,0,1] row_mask:0xf bank_mask:0xf
	v_cmp_eq_u32_e32 vcc, 0, v17
	s_movk_i32 s45, 0xe0
	v_cmp_gt_u32_e64 s[60:61], s45, v10
	v_add_u32_e32 v11, -1, v42
	v_ffbh_u32_e32 v11, v11
	s_and_b64 vcc, vcc, s[60:61]
	s_and_saveexec_b64 s[60:61], vcc
	v_sub_u32_e32 v11, 32, v11
	v_cmp_lt_u32_e32 vcc, 1, v42
	v_lshlrev_b32_e32 v44, 4, v43
	v_add_u32_e32 v44, 0x1ce00, v44
	v_cndmask_b32_e32 v11, 0, v11, vcc
	v_lshlrev_b32_e32 v11, 23, v11
	v_mov_b32_e32 v45, v42
	v_sub_u32_e32 v49, 0x46800000, v11
	v_add_u32_e32 v12, 0x38000000, v11
	v_cvt_f32_u32_e32 v48, v42
	v_mul_f32_e32 v12, v12, v20
	v_mul_f32_e32 v46, v40, v49
	v_mul_f32_e32 v47, v41, v49
	v_mul_f32_e32 v48, v48, v49
	v_lshlrev_b32_e32 v13, 3, v10
	v_add_u32_e32 v13, 0x22c60, v13
	ds_write_b64 v13, v[44:45]
	v_lshlrev_b32_e32 v13, 4, v10
	v_add_u32_e32 v13, 0x23360, v13
	ds_write_b128 v13, v[46:49]
	v_lshlrev_b32_e32 v13, 2, v10
	v_add_u32_e32 v13, 0x22200, v13
	ds_write_b32 v13, v12
	v_cmp_gt_u32_e32 vcc, s3, v10
	v_cmp_lt_u32_e64 s[46:47], 16, v42
	v_mov_b32_e32 v14, 0x24864
	v_mov_b32_e32 v15, 0x24860
	v_mov_b32_e32 v16, 0x244e0
	v_mov_b32_e32 v36, 0x24160
	s_and_b64 exec, exec, vcc
	v_cndmask_b32_e64 v14, v14, v15, s[46:47]
	v_cndmask_b32_e64 v16, v16, v36, s[46:47]
	ds_add_rtn_u32 v15, v14, v60
	s_waitcnt lgkmcnt(0)
	v_lshl_add_u32 v15, v15, 2, v16
	ds_write_b32 v15, v10
	s_mov_b64 exec, s[60:61]
	s_waitcnt lgkmcnt(0)
	s_barrier
	v_mov_b32_e32 v11, 0x24860
	ds_read_b64 v[12:13], v11
	v_mov_b32_e32 v61, 0x22c60
	v_mov_b32_e32 v62, 0x23360
	v_cmp_gt_u32_e32 vcc, 32, v18
	v_mov_b32_e32 v2, v55
	s_nop 0
	v_cndmask_b32_e64 v63, 0, -1, vcc
	s_waitcnt lgkmcnt(0)
	v_readfirstlane_b32 s62, v12
	v_readfirstlane_b32 s63, v13
	s_add_i32 s62, s62, 1
	s_lshr_b32 s62, s62, 1
	s_add_i32 s63, s63, 1
	s_lshr_b32 s63, s63, 1
.Lp_next:
	s_mov_b64 exec, 1
	ds_add_rtn_u32 v10, v59, v60
	s_mov_b64 exec, -1
	s_waitcnt lgkmcnt(0)
	v_readfirstlane_b32 s34, v10
	s_cmp_lt_u32 s34, s62
	s_cselect_b32 s45, s64, s65
	s_cselect_b32 s46, 0, s62
	s_cselect_b32 s48, s62, s63
	s_sub_u32 s47, s34, s46
	s_cmp_ge_u32 s47, s48
	s_cbranch_scc1 .Lp_done
	s_lshl_b32 s47, s47, 3
	s_add_u32 s45, s45, s47
	v_mov_b32_e32 v11, s45
	ds_read2_b32 v[12:13], v11 offset1:1
	s_waitcnt lgkmcnt(0)
	v_readfirstlane_b32 s35, v12
	v_readfirstlane_b32 s36, v13
	s_nop 1
	v_mov_b32_e32 v10, s35
	v_mov_b32_e32 v11, s36
	v_cndmask_b32_e64 v12, v10, v11, s[54:55]
	v_cndmask_b32_e64 v13, v10, v11, s[56:57]
	v_lshl_add_u32 v12, v12, 3, v61
	v_lshl_add_u32 v14, v13, 4, v62
	ds_read_b64 v[2:3], v12
	ds_read_b128 v[4:7], v14
	v_mad_u32_u24 v9, v13, s49, v58
	v_mov_b32_e32 v8, v56
	v_mov_b32_e32 v24, 0
	v_mov_b32_e32 v25, 0
	v_mov_b32_e32 v26, 0
	v_mov_b32_e32 v27, 0
	v_mov_b32_e32 v28, 0
	v_mov_b32_e32 v29, 0
	v_mov_b32_e32 v30, 0
	v_mov_b32_e32 v31, 0
	s_waitcnt lgkmcnt(0)
	v_add_u32_e32 v2, v2, v55
	v_and_b32_e32 v3, v3, v63
	s_nop 0
	v_readlane_b32 s41, v3, 0
	v_readlane_b32 s42, v3, 4
	s_add_i32 s41, s41, 15
	s_lshr_b32 s41, s41, 4
	s_add_i32 s42, s42, 15
	s_lshr_b32 s42, s42, 4
	s_max_u32 s43, s41, s42
	s_cmp_eq_u32 s43, 0
	s_cbranch_scc1 .Lp_fin
	s_mov_b32 s44, 0
.Lsub:
	ds_read_b64 v[36:37], v2
	v_cmp_gt_u32_e32 vcc, v3, v8
	v_add_u32_e32 v2, 64, v2
	v_add_u32_e32 v8, 16, v8
	v_mov_b32_e32 v33, 0x3c00
	s_waitcnt lgkmcnt(0)
	v_perm_b32 v32, v37, v36, v57
	v_cndmask_b32_e32 v33, 0, v33, vcc
	s_nop 0
	v_cndmask_b32_e32 v32, 0, v32, vcc
	s_nop 1
	v_mfma_f32_32x32x16_f16 v[96:111], v[32:35], v[64:67], 0
	v_mfma_f32_32x32x16_f16 v[112:127], v[32:35], v[68:71], 0
	s_nop 10
	v_add_f32_e64 v38, |v96|, |v97|
	v_add_f32_e64 v39, |v98|, |v99|
	v_add_f32_e64 v38, v38, |v100|
	v_add_f32_e64 v39, v39, |v101|
	v_add_f32_e64 v38, v38, |v102|
	v_add_f32_e64 v39, v39, |v103|
	v_add_f32_e64 v38, v38, |v104|
	v_add_f32_e64 v39, v39, |v105|
	v_add_f32_e64 v38, v38, |v106|
	v_add_f32_e64 v39, v39, |v107|
	v_add_f32_e64 v38, v38, |v108|
	v_add_f32_e64 v39, v39, |v109|
	v_add_f32_e64 v38, v38, |v110|
	v_add_f32_e64 v39, v39, |v111|
	v_add_f32_e32 v38, v38, v39
	v_add_f32_e32 v24, v24, v38
	v_mfma_f32_32x32x16_f16 v[96:111], v[32:35], v[72:75], 0
	v_add_f32_e64 v38, |v112|, |v113|
	v_add_f32_e64 v39, |v114|, |v115|
	v_add_f32_e64 v38, v38, |v116|
	v_add_f32_e64 v39, v39, |v117|
	v_add_f32_e64 v38, v38, |v118|
	v_add_f32_e64 v39, v39, |v119|
	v_add_f32_e64 v38, v38, |v120|
	v_add_f32_e64 v39, v39, |v121|
	v_add_f32_e64 v38, v38, |v122|
	v_add_f32_e64 v39, v39, |v123|
	v_add_f32_e64 v38, v38, |v124|
	v_add_f32_e64 v39, v39, |v125|
	v_add_f32_e64 v38, v38, |v126|
	v_add_f32_e64 v39, v39, |v127|
	v_add_f32_e32 v38, v38, v39
	v_add_f32_e32 v25, v25, v38
	v_mfma_f32_32x32x16_f16 v[112:127], v[32:35], v[76:79], 0
	v_add_f32_e64 v38, |v96|, |v97|
	v_add_f32_e64 v39, |v98|, |v99|
	v_add_f32_e64 v38, v38, |v100|
	v_add_f32_e64 v39, v39, |v101|
	v_add_f32_e64 v38, v38, |v102|
	v_add_f32_e64 v39, v39, |v103|
	v_add_f32_e64 v38, v38, |v104|
	v_add_f32_e64 v39, v39, |v105|
	v_add_f32_e64 v38, v38, |v106|
	v_add_f32_e64 v39, v39, |v107|
	v_add_f32_e64 v38, v38, |v108|
	v_add_f32_e64 v39, v39, |v109|
	v_add_f32_e64 v38, v38, |v110|
	v_add_f32_e64 v39, v39, |v111|
	v_add_f32_e32 v38, v38, v39
	v_add_f32_e32 v26, v26, v38
	v_mfma_f32_32x32x16_f16 v[96:111], v[32:35], v[80:83], 0
	v_add_f32_e64 v38, |v112|, |v113|
	v_add_f32_e64 v39, |v114|, |v115|
	v_add_f32_e64 v38, v38, |v116|
	v_add_f32_e64 v39, v39, |v117|
	v_add_f32_e64 v38, v38, |v118|
	v_add_f32_e64 v39, v39, |v119|
	v_add_f32_e64 v38, v38, |v120|
	v_add_f32_e64 v39, v39, |v121|
	v_add_f32_e64 v38, v38, |v122|
	v_add_f32_e64 v39, v39, |v123|
	v_add_f32_e64 v38, v38, |v124|
	v_add_f32_e64 v39, v39, |v125|
	v_add_f32_e64 v38, v38, |v126|
	v_add_f32_e64 v39, v39, |v127|
	v_add_f32_e32 v38, v38, v39
	v_add_f32_e32 v27, v27, v38
	v_mfma_f32_32x32x16_f16 v[112:127], v[32:35], v[84:87], 0
	v_add_f32_e64 v38, |v96|, |v97|
	v_add_f32_e64 v39, |v98|, |v99|
	v_add_f32_e64 v38, v38, |v100|
	v_add_f32_e64 v39, v39, |v101|
	v_add_f32_e64 v38, v38, |v102|
	v_add_f32_e64 v39, v39, |v103|
	v_add_f32_e64 v38, v38, |v104|
	v_add_f32_e64 v39, v39, |v105|
	v_add_f32_e64 v38, v38, |v106|
	v_add_f32_e64 v39, v39, |v107|
	v_add_f32_e64 v38, v38, |v108|
	v_add_f32_e64 v39, v39, |v109|
	v_add_f32_e64 v38, v38, |v110|
	v_add_f32_e64 v39, v39, |v111|
	v_add_f32_e32 v38, v38, v39
	v_add_f32_e32 v28, v28, v38
	v_mfma_f32_32x32x16_f16 v[96:111], v[32:35], v[88:91], 0
	v_add_f32_e64 v38, |v112|, |v113|
	v_add_f32_e64 v39, |v114|, |v115|
	v_add_f32_e64 v38, v38, |v116|
	v_add_f32_e64 v39, v39, |v117|
	v_add_f32_e64 v38, v38, |v118|
	v_add_f32_e64 v39, v39, |v119|
	v_add_f32_e64 v38, v38, |v120|
	v_add_f32_e64 v39, v39, |v121|
	v_add_f32_e64 v38, v38, |v122|
	v_add_f32_e64 v39, v39, |v123|
	v_add_f32_e64 v38, v38, |v124|
	v_add_f32_e64 v39, v39, |v125|
	v_add_f32_e64 v38, v38, |v126|
	v_add_f32_e64 v39, v39, |v127|
	v_add_f32_e32 v38, v38, v39
	v_add_f32_e32 v29, v29, v38
	v_mfma_f32_32x32x16_f16 v[112:127], v[32:35], v[92:95], 0
	v_add_f32_e64 v38, |v96|, |v97|
	v_add_f32_e64 v39, |v98|, |v99|
	v_add_f32_e64 v38, v38, |v100|
	v_add_f32_e64 v39, v39, |v101|
	v_add_f32_e64 v38, v38, |v102|
	v_add_f32_e64 v39, v39, |v103|
	v_add_f32_e64 v38, v38, |v104|
	v_add_f32_e64 v39, v39, |v105|
	v_add_f32_e64 v38, v38, |v106|
	v_add_f32_e64 v39, v39, |v107|
	v_add_f32_e64 v38, v38, |v108|
	v_add_f32_e64 v39, v39, |v109|
	v_add_f32_e64 v38, v38, |v110|
	v_add_f32_e64 v39, v39, |v111|
	v_add_f32_e32 v38, v38, v39
	v_add_f32_e32 v30, v30, v38
	v_add_f32_e64 v38, |v112|, |v113|
	v_add_f32_e64 v39, |v114|, |v115|
	v_add_f32_e64 v38, v38, |v116|
	v_add_f32_e64 v39, v39, |v117|
	v_add_f32_e64 v38, v38, |v118|
	v_add_f32_e64 v39, v39, |v119|
	v_add_f32_e64 v38, v38, |v120|
	v_add_f32_e64 v39, v39, |v121|
	v_add_f32_e64 v38, v38, |v122|
	v_add_f32_e64 v39, v39, |v123|
	v_add_f32_e64 v38, v38, |v124|
	v_add_f32_e64 v39, v39, |v125|
	v_add_f32_e64 v38, v38, |v126|
	v_add_f32_e64 v39, v39, |v127|
	v_add_f32_e32 v38, v38, v39
	v_add_f32_e32 v31, v31, v38
	s_add_i32 s44, s44, 1
	s_cmp_lt_u32 s44, s43
	s_cbranch_scc1 .Lsub
.Lp_fin:
	v_mul_f32_e32 v40, v7, v24
	v_fma_mix_f32 v40, v6, v65, v40 op_sel_hi:[0,1,0]
	v_fma_mix_f32 v40, v5, v64, v40 op_sel:[0,1,0] op_sel_hi:[0,1,0]
	v_fma_mixlo_f16 v40, v4, v64, v40 op_sel_hi:[0,1,0]
	ds_write_b16 v9, v40 offset:0
	v_mul_f32_e32 v41, v7, v25
	v_fma_mix_f32 v41, v6, v69, v41 op_sel_hi:[0,1,0]
	v_fma_mix_f32 v41, v5, v68, v41 op_sel:[0,1,0] op_sel_hi:[0,1,0]
	v_fma_mixlo_f16 v41, v4, v68, v41 op_sel_hi:[0,1,0]
	ds_write_b16 v9, v41 offset:64
	v_mul_f32_e32 v40, v7, v26
	v_fma_mix_f32 v40, v6, v73, v40 op_sel_hi:[0,1,0]
	v_fma_mix_f32 v40, v5, v72, v40 op_sel:[0,1,0] op_sel_hi:[0,1,0]
	v_fma_mixlo_f16 v40, v4, v72, v40 op_sel_hi:[0,1,0]
	ds_write_b16 v9, v40 offset:128
	v_mul_f32_e32 v41, v7, v27
	v_fma_mix_f32 v41, v6, v77, v41 op_sel_hi:[0,1,0]
	v_fma_mix_f32 v41, v5, v76, v41 op_sel:[0,1,0] op_sel_hi:[0,1,0]
	v_fma_mixlo_f16 v41, v4, v76, v41 op_sel_hi:[0,1,0]
	ds_write_b16 v9, v41 offset:192
	v_mul_f32_e32 v40, v7, v28
	v_fma_mix_f32 v40, v6, v81, v40 op_sel_hi:[0,1,0]
	v_fma_mix_f32 v40, v5, v80, v40 op_sel:[0,1,0] op_sel_hi:[0,1,0]
	v_fma_mixlo_f16 v40, v4, v80, v40 op_sel_hi:[0,1,0]
	ds_write_b16 v9, v40 offset:256
	v_mul_f32_e32 v41, v7, v29
	v_fma_mix_f32 v41, v6, v85, v41 op_sel_hi:[0,1,0]
	v_fma_mix_f32 v41, v5, v84, v41 op_sel:[0,1,0] op_sel_hi:[0,1,0]
	v_fma_mixlo_f16 v41, v4, v84, v41 op_sel_hi:[0,1,0]
	ds_write_b16 v9, v41 offset:320
	v_mul_f32_e32 v40, v7, v30
	v_fma_mix_f32 v40, v6, v89, v40 op_sel_hi:[0,1,0]
	v_fma_mix_f32 v40, v5, v88, v40 op_sel:[0,1,0] op_sel_hi:[0,1,0]
	v_fma_mixlo_f16 v40, v4, v88, v40 op_sel_hi:[0,1,0]
	ds_write_b16 v9, v40 offset:384
	v_mul_f32_e32 v41, v7, v31
	v_fma_mix_f32 v41, v6, v93, v41 op_sel_hi:[0,1,0]
	v_fma_mix_f32 v41, v5, v92, v41 op_sel:[0,1,0] op_sel_hi:[0,1,0]
	v_fma_mixlo_f16 v41, v4, v92, v41 op_sel_hi:[0,1,0]
	ds_write_b16 v9, v41 offset:448
	s_branch .Lp_next

	.amdhsa_kernel _Z6k_mainPKiPKjPK15HIP_vector_typeIfLj2EEPKfS8_PKDF16_S8_Pf
		.amdhsa_group_segment_fixed_size 151664
		.amdhsa_private_segment_fixed_size 0
		.amdhsa_kernarg_size 64
		.amdhsa_user_sgpr_count 2
		.amdhsa_user_sgpr_dispatch_ptr 0
		.amdhsa_user_sgpr_queue_ptr 0
		.amdhsa_user_sgpr_kernarg_segment_ptr 1
		.amdhsa_user_sgpr_dispatch_id 0
		.amdhsa_user_sgpr_kernarg_preload_length 0
		.amdhsa_user_sgpr_kernarg_preload_offset 0
		.amdhsa_user_sgpr_private_segment_size 0
		.amdhsa_uses_dynamic_stack 0
		.amdhsa_enable_private_segment 0
		.amdhsa_system_sgpr_workgroup_id_x 1
		.amdhsa_system_sgpr_workgroup_id_y 0
		.amdhsa_system_sgpr_workgroup_id_z 0
		.amdhsa_system_sgpr_workgroup_info 0
		.amdhsa_system_vgpr_workitem_id 0
		.amdhsa_next_free_vgpr 128
		.amdhsa_next_free_sgpr 96
		.amdhsa_accum_offset 128
		.amdhsa_reserve_vcc 1
		.amdhsa_float_round_mode_32 0
		.amdhsa_float_round_mode_16_64 0
		.amdhsa_float_denorm_mode_32 3
		.amdhsa_float_denorm_mode_16_64 3
		.amdhsa_dx10_clamp 1
		.amdhsa_ieee_mode 1
		.amdhsa_fp16_overflow 0
		.amdhsa_tg_split 0
		.amdhsa_exception_fp_ieee_invalid_op 0
		.amdhsa_exception_fp_denorm_src 0
		.amdhsa_exception_fp_ieee_div_zero 0
		.amdhsa_exception_fp_ieee_overflow 0
		.amdhsa_exception_fp_ieee_underflow 0
		.amdhsa_exception_fp_ieee_inexact 0
		.amdhsa_exception_int_div_zero 0
	.end_amdhsa_kernel

amdhsa.kernels:
  - .agpr_count:     0
    .args:
      - .actual_access:  read_only
        .address_space:  global
        .offset:         0
        .size:           8
        .value_kind:     global_buffer
      - .actual_access:  read_only
        .address_space:  global
        .offset:         8
        .size:           8
        .value_kind:     global_buffer
      - .actual_access:  write_only
        .address_space:  global
        .offset:         16
        .size:           8
        .value_kind:     global_buffer
      - .actual_access:  write_only
        .address_space:  global
        .offset:         24
        .size:           8
        .value_kind:     global_buffer
      - .actual_access:  write_only
        .address_space:  global
        .offset:         32
        .size:           8
        .value_kind:     global_buffer
      - .actual_access:  write_only
        .address_space:  global
        .offset:         40
        .size:           8
        .value_kind:     global_buffer
      - .actual_access:  write_only
        .address_space:  global
        .offset:         48
        .size:           8
        .value_kind:     global_buffer
      - .actual_access:  write_only
        .address_space:  global
        .offset:         56
        .size:           8
        .value_kind:     global_buffer
      - .actual_access:  read_only
        .address_space:  global
        .offset:         64
        .size:           8
        .value_kind:     global_buffer
      - .actual_access:  write_only
        .address_space:  global
        .offset:         72
        .size:           8
        .value_kind:     global_buffer
    .group_segment_fixed_size: 18800
    .kernarg_segment_align: 8
    .kernarg_segment_size: 80
    .language:       OpenCL C
    .language_version:
      - 2
      - 0
    .max_flat_workgroup_size: 1024
    .name:           _Z6k_partPKiS0_PjPhS1_S1_PfS3_PKfPDF16_
    .private_segment_fixed_size: 0
    .sgpr_count:     48
    .sgpr_spill_count: 0
    .symbol:         _Z6k_partPKiS0_PjPhS1_S1_PfS3_PKfPDF16_.kd
    .uniform_work_group_size: 1
    .uses_dynamic_stack: false
    .vgpr_count:     40
    .vgpr_spill_count: 0
    .wavefront_size: 64
  - .agpr_count:     0
    .args:
      - .actual_access:  read_only
        .address_space:  global
        .offset:         0
        .size:           8
        .value_kind:     global_buffer
      - .actual_access:  read_only
        .address_space:  global
        .offset:         8
        .size:           8
        .value_kind:     global_buffer
      - .actual_access:  read_only
        .address_space:  global
        .offset:         16
        .size:           8
        .value_kind:     global_buffer
      - .actual_access:  read_only
        .address_space:  global
        .offset:         24
        .size:           8
        .value_kind:     global_buffer
      - .actual_access:  write_only
        .address_space:  global
        .offset:         32
        .size:           8
        .value_kind:     global_buffer
      - .actual_access:  write_only
        .address_space:  global
        .offset:         40
        .size:           8
        .value_kind:     global_buffer
    .group_segment_fixed_size: 3076
    .kernarg_segment_align: 8
    .kernarg_segment_size: 48
    .language:       OpenCL C
    .language_version:
      - 2
      - 0
    .max_flat_workgroup_size: 512
    .name:           _Z5k_degPKjPKhS0_S0_P15HIP_vector_typeIiLj2EEPi
    .private_segment_fixed_size: 0
    .sgpr_count:     74
    .sgpr_spill_count: 0
    .symbol:         _Z5k_degPKjPKhS0_S0_P15HIP_vector_typeIiLj2EEPi.kd
    .uniform_work_group_size: 1
    .uses_dynamic_stack: false
    .vgpr_count:     61
    .vgpr_spill_count: 0
    .wavefront_size: 64
  - .agpr_count:     0
    .args:
      - .actual_access:  read_only
        .address_space:  global
        .offset:         0
        .size:           8
        .value_kind:     global_buffer
      - .actual_access:  read_only
        .address_space:  global
        .offset:         8
        .size:           8
        .value_kind:     global_buffer
      - .actual_access:  read_only
        .address_space:  global
        .offset:         16
        .size:           8
        .value_kind:     global_buffer
      - .actual_access:  read_only
        .address_space:  global
        .offset:         24
        .size:           8
        .value_kind:     global_buffer
      - .actual_access:  write_only
        .address_space:  global
        .offset:         32
        .size:           8
        .value_kind:     global_buffer
      - .actual_access:  write_only
        .address_space:  global
        .offset:         40
        .size:           8
        .value_kind:     global_buffer
      - .actual_access:  write_only
        .address_space:  global
        .offset:         48
        .size:           8
        .value_kind:     global_buffer
    .group_segment_fixed_size: 4128
    .kernarg_segment_align: 8
    .kernarg_segment_size: 56
    .language:       OpenCL C
    .language_version:
      - 2
      - 0
    .max_flat_workgroup_size: 256
    .name:           _Z5k_csrPKjS0_PK15HIP_vector_typeIiLj2EEPKiPiPjPS1_IfLj2EE
    .private_segment_fixed_size: 0
    .sgpr_count:     74
    .sgpr_spill_count: 0
    .symbol:         _Z5k_csrPKjS0_PK15HIP_vector_typeIiLj2EEPKiPiPjPS1_IfLj2EE.kd
    .uniform_work_group_size: 1
    .uses_dynamic_stack: false
    .vgpr_count:     122
    .vgpr_spill_count: 0
    .wavefront_size: 64
  - .agpr_count:     0
    .args:
      - .actual_access:  read_only
        .address_space:  global
        .offset:         0
        .size:           8
        .value_kind:     global_buffer
      - .actual_access:  read_only
        .address_space:  global
        .offset:         8
        .size:           8
        .value_kind:     global_buffer
      - .actual_access:  read_only
        .address_space:  global
        .offset:         16
        .size:           8
        .value_kind:     global_buffer
      - .actual_access:  read_only
        .address_space:  global
        .offset:         24
        .size:           8
        .value_kind:     global_buffer
      - .actual_access:  read_only
        .address_space:  global
        .offset:         32
        .size:           8
        .value_kind:     global_buffer
      - .actual_access:  read_only
        .address_space:  global
        .offset:         40
        .size:           8
        .value_kind:     global_buffer
      - .actual_access:  read_only
        .address_space:  global
        .offset:         48
        .size:           8
        .value_kind:     global_buffer
      - .address_space:  global
        .offset:         56
        .size:           8
        .value_kind:     global_buffer
    .group_segment_fixed_size: 151664
    .kernarg_segment_align: 8
    .kernarg_segment_size: 64
    .language:       OpenCL C
    .language_version:
      - 2
      - 0
    .max_flat_workgroup_size: 1024
    .name:           _Z6k_mainPKiPKjPK15HIP_vector_typeIfLj2EEPKfS8_PKDF16_S8_Pf
    .private_segment_fixed_size: 0
    .sgpr_count:     84
    .sgpr_spill_count: 0
    .symbol:         _Z6k_mainPKiPKjPK15HIP_vector_typeIfLj2EEPKfS8_PKDF16_S8_Pf.kd
    .uniform_work_group_size: 1
    .uses_dynamic_stack: false
    .vgpr_count:     128
    .vgpr_spill_count: 0
    .wavefront_size: 64
  - .agpr_count:     0
    .args:
      - .actual_access:  read_only
        .address_space:  global
        .offset:         0
        .size:           8
        .value_kind:     global_buffer
      - .actual_access:  read_only
        .address_space:  global
        .offset:         8
        .size:           8
        .value_kind:     global_buffer
      - .actual_access:  read_only
        .address_space:  global
        .offset:         16
        .size:           8
        .value_kind:     global_buffer
      - .actual_access:  read_only
        .address_space:  global
        .offset:         24
        .size:           8
        .value_kind:     global_buffer
      - .actual_access:  read_only
        .address_space:  global
        .offset:         32
        .size:           8
        .value_kind:     global_buffer
      - .actual_access:  read_only
        .address_space:  global
        .offset:         40
        .size:           8
        .value_kind:     global_buffer
      - .actual_access:  read_only
        .address_space:  global
        .offset:         48
        .size:           8
        .value_kind:     global_buffer
      - .actual_access:  read_only
        .address_space:  global
        .offset:         56
        .size:           8
        .value_kind:     global_buffer
      - .actual_access:  read_only
        .address_space:  global
        .offset:         64
        .size:           8
        .value_kind:     global_buffer
      - .actual_access:  read_only
        .address_space:  global
        .offset:         72
        .size:           8
        .value_kind:     global_buffer
      - .address_space:  global
        .offset:         80
        .size:           8
        .value_kind:     global_buffer
    .group_segment_fixed_size: 2688
    .kernarg_segment_align: 8
    .kernarg_segment_size: 88
    .language:       OpenCL C
    .language_version:
      - 2
      - 0
    .max_flat_workgroup_size: 256
    .name:           _Z7k_finalPKfS0_S0_S0_S0_S0_S0_S0_S0_S0_Pf
    .private_segment_fixed_size: 0
    .sgpr_count:     36
    .sgpr_spill_count: 0
    .symbol:         _Z7k_finalPKfS0_S0_S0_S0_S0_S0_S0_S0_S0_Pf.kd
    .uniform_work_group_size: 1
    .uses_dynamic_stack: false
    .vgpr_count:     98
    .vgpr_spill_count: 0
    .wavefront_size: 64
